# E row loop: dead SGPR-tuple reloads removed (56 v_readlane per row)
# speedup vs baseline: 1.0240x; 1.0008x over previous
; __device__ void phase_E_rows(const Params& p, int l, char* smem, int vb, int nvb, bool split, int nrows, int oz) {
;     ...
;         if (row + 2 < rend) E2_LOAD(nx1, nxb1, ny1, row + 2)
.LBB0_932:
	s_add_i32 s28, s56, 2
	s_cmp_ge_i32 s28, s27
	s_cbranch_scc1 .LBB0_957
	s_cmpk_lt_i32 s56, 0x3ffe
	s_mov_b64 s[80:81], -1
	s_cselect_b64 s[82:83], -1, 0
	s_and_b64 vcc, exec, s[0:1]
	s_cbranch_vccz .LBB0_939
	s_and_b64 vcc, exec, s[82:83]
	s_cbranch_vccz .LBB0_936
	s_ashr_i32 s29, s28, 31
	v_readlane_b32 s18, v253, 32
	v_readlane_b32 s19, v253, 33
	s_mov_b64 s[80:81], 0
	s_mov_b64 s[46:47], s[18:19]
	s_mov_b64 s[18:19], s[88:89]
	s_mov_b64 s[84:85], s[28:29]

.LBB0_939:
	s_andn2_b64 vcc, exec, s[80:81]
	s_cbranch_vccnz .LBB0_944
	s_and_b64 vcc, exec, s[82:83]
	s_cbranch_vccz .LBB0_942
	v_readlane_b32 s4, v253, 40
	s_ashr_i32 s29, s28, 31
	v_readlane_b32 s5, v253, 41
	s_mov_b64 s[46:47], s[4:5]
	s_mov_b64 s[84:85], s[28:29]
	s_mov_b64 s[18:19], s[88:89]
	s_cbranch_execz .LBB0_943
	s_branch .LBB0_944
.LBB0_942:
	v_readlane_b32 s8, v253, 44
	v_readlane_b32 s9, v253, 45
	s_mov_b64 s[46:47], s[8:9]
	s_mov_b64 s[18:19], s[88:89]

; __device__ __forceinline__ float h_lo(unsigned u) { return (float)__builtin_bit_cast(f16v2, u)[0]; }
; __device__ void phase_E_rows(const Params& p, int l, char* smem, int vb, int nvb, bool split, int nrows, int oz) {
;     ...
;         float4 xv[4];
;         u32x4 yq[2];
; #pragma unroll
;         for (int k = 0; k < 4; ++k) {
;             const u32x4 w = nxb0[k >> 1];
;             const int h2 = 2 * (k & 1);
;             xv[k] = (l <= 1) ? nx0[k] : make_float4(h_lo(w[h2]), h_hi(w[h2]), h_lo(w[h2 + 1]), h_hi(w[h2 + 1]));
;         }
; #pragma unroll
;         for (int k = 0; k < 4; ++k) nx0[k] = nx1[k];
; #pragma unroll
;         for (int k2 = 0; k2 < 2; ++k2) { yq[k2] = ny0[k2]; nxb0[k2] = nxb1[k2]; ny0[k2] = ny1[k2]; }
;         if (row + 2 < rend) E2_LOAD(nx1, nxb1, ny1, row + 2)
;         float y[4][4];
;         float ss = 0.f;
; #pragma unroll
;         for (int k = 0; k < 4; ++k) {
;             { const u32x4 w = yq[k >> 1]; const int h2 = 2 * (k & 1); y[k][0] = lo16(w[h2]); y[k][1] = hi16(w[h2]); y[k][2] = lo16(w[h2 + 1]); y[k][3] = hi16(w[h2 + 1]); }
;             ss += y[k][0] * y[k][0] + y[k][1] * y[k][1] + y[k][2] * y[k][2] + y[k][3] * y[k][3];
;         }
;         float rs = 0.f;
;         if (l > 0) {
;             ss = wave_sum(ss);
;             rs = rsqrtf(ss * (1.f / DM) + EPS);
;         }
;         float ss2 = 0.f;
; #pragma unroll
;         for (int k = 0; k < 4; ++k) {
;             if (l > 0) {
;                 xv[k].x += gp[k].x * (y[k][0] * rs);
;                 xv[k].y += gp[k].y * (y[k][1] * rs);
;                 xv[k].z += gp[k].z * (y[k][2] * rs);
;                 xv[k].w += gp[k].w * (y[k][3] * rs);
;             }
;             ss2 += xv[k].x * xv[k].x + xv[k].y * xv[k].y + xv[k].z * xv[k].z + xv[k].w * xv[k].w;
;         }
;         if (l > 0) {
;             const __amdgpu_buffer_rsrc_t xr = __builtin_amdgcn_make_buffer_rsrc((void*)xcur, (short)0, 4096, 0x00020000);
; #pragma unroll
;             for (int k2 = 0; k2 < 2; ++k2) {
;                 const u32x4 xb = {pk_h2(xv[2 * k2].x, xv[2 * k2].y), pk_h2(xv[2 * k2].z, xv[2 * k2].w), pk_h2(xv[2 * k2 + 1].x, xv[2 * k2 + 1].y), pk_h2(xv[2 * k2 + 1].z, xv[2 * k2 + 1].w)};
;                 __builtin_amdgcn_raw_buffer_store_b128(xb, xr, 2048 + (k2 * 512 + lane * 8) * 2, 0, 16);
;             }
.LBB0_960:
	v_cvt_f32_f16_e32 v47, v25
	v_cvt_f32_f16_sdwa v25, v25 dst_sel:DWORD dst_unused:UNUSED_PAD src0_sel:WORD_1
	v_cvt_f32_f16_e32 v107, v24
	v_cvt_f32_f16_sdwa v109, v24 dst_sel:DWORD dst_unused:UNUSED_PAD src0_sel:WORD_1
	v_cndmask_b32_e64 v24, v47, v42, s[38:39]
	v_cndmask_b32_e64 v25, v25, v43, s[38:39]
	v_cvt_f32_f16_e32 v42, v27
	v_cvt_f32_f16_sdwa v27, v27 dst_sel:DWORD dst_unused:UNUSED_PAD src0_sel:WORD_1
	v_cvt_f32_f16_e32 v43, v26
	v_cvt_f32_f16_sdwa v26, v26 dst_sel:DWORD dst_unused:UNUSED_PAD src0_sel:WORD_1
	v_cndmask_b32_e64 v40, v107, v40, s[38:39]
	v_cndmask_b32_e64 v39, v27, v39, s[38:39]
	v_cvt_f32_f16_e32 v27, v20
	v_cndmask_b32_e64 v37, v26, v37, s[38:39]
	v_cvt_f32_f16_e32 v26, v21
	v_cvt_f32_f16_sdwa v21, v21 dst_sel:DWORD dst_unused:UNUSED_PAD src0_sel:WORD_1
	v_cvt_f32_f16_sdwa v20, v20 dst_sel:DWORD dst_unused:UNUSED_PAD src0_sel:WORD_1
	v_cndmask_b32_e64 v41, v109, v41, s[38:39]
	v_cndmask_b32_e64 v38, v42, v38, s[38:39]
	v_cndmask_b32_e64 v35, v21, v35, s[38:39]
	v_cndmask_b32_e64 v33, v20, v33, s[38:39]
	v_cvt_f32_f16_e32 v20, v23
	v_cvt_f32_f16_sdwa v21, v23 dst_sel:DWORD dst_unused:UNUSED_PAD src0_sel:WORD_1
	v_cvt_f32_f16_e32 v23, v22
	v_cvt_f32_f16_sdwa v22, v22 dst_sel:DWORD dst_unused:UNUSED_PAD src0_sel:WORD_1
	v_cndmask_b32_e64 v36, v43, v36, s[38:39]
	v_cndmask_b32_e64 v42, v20, v30, s[38:39]
	v_cndmask_b32_e64 v43, v21, v31, s[38:39]
	v_pk_mul_f32 v[20:21], v[46:47], v[174:175] op_sel_hi:[0,1]
	v_cndmask_b32_e64 v176, v23, v28, s[38:39]
	v_cndmask_b32_e64 v177, v22, v29, s[38:39]
	v_pk_fma_f32 v[22:23], v[118:119], v[20:21], v[40:41]
	v_pk_mul_f32 v[20:21], v[46:47], v[172:173] op_sel_hi:[0,1]
	v_cndmask_b32_e64 v34, v26, v34, s[38:39]
	v_cndmask_b32_e64 v32, v27, v32, s[38:39]
	v_pk_fma_f32 v[20:21], v[120:121], v[20:21], v[24:25]
	v_cndmask_b32_e64 v27, v41, v23, s[36:37]
	v_cndmask_b32_e64 v26, v40, v22, s[36:37]
	v_pk_mul_f32 v[22:23], v[46:47], v[170:171] op_sel_hi:[0,1]
	v_cndmask_b32_e64 v21, v25, v21, s[36:37]
	v_cndmask_b32_e64 v20, v24, v20, s[36:37]
	v_pk_fma_f32 v[24:25], v[122:123], v[22:23], v[36:37]
	v_pk_mul_f32 v[22:23], v[46:47], v[168:169] op_sel_hi:[0,1]
	v_cndmask_b32_e64 v31, v37, v25, s[36:37]
	v_cndmask_b32_e64 v30, v36, v24, s[36:37]
	v_pk_mul_f32 v[24:25], v[46:47], v[166:167] op_sel_hi:[0,1]
	v_pk_fma_f32 v[28:29], v[126:127], v[24:25], v[32:33]
	v_pk_mul_f32 v[24:25], v[46:47], v[50:51] op_sel_hi:[0,1]
	v_pk_fma_f32 v[24:25], v[128:129], v[24:25], v[34:35]
	v_cndmask_b32_e64 v33, v33, v29, s[36:37]
	v_cndmask_b32_e64 v32, v32, v28, s[36:37]
	v_pk_mul_f32 v[28:29], v[46:47], v[48:49] op_sel_hi:[0,1]
	v_cndmask_b32_e64 v25, v35, v25, s[36:37]
	v_cndmask_b32_e64 v24, v34, v24, s[36:37]
	v_pk_fma_f32 v[34:35], v[134:135], v[28:29], v[176:177]
	v_pk_mul_f32 v[28:29], v[46:47], v[44:45] op_sel_hi:[0,1]
	v_pk_fma_f32 v[22:23], v[124:125], v[22:23], v[38:39]
	v_pk_fma_f32 v[28:29], v[136:137], v[28:29], v[42:43]
	v_cndmask_b32_e64 v23, v39, v23, s[36:37]
	v_cndmask_b32_e64 v22, v38, v22, s[36:37]
	v_cndmask_b32_e64 v29, v43, v29, s[36:37]
	v_cndmask_b32_e64 v28, v42, v28, s[36:37]
	v_cndmask_b32_e64 v35, v177, v35, s[36:37]
	s_and_b64 vcc, exec, s[44:45]
	v_cndmask_b32_e64 v34, v176, v34, s[36:37]
	s_cbranch_vccnz .LBB0_962
	s_add_i32 s28, s56, 0xffffc000
	s_and_b64 s[20:21], s[20:21], exec
	s_cselect_b32 s21, 0, s57
	s_cselect_b32 s20, s28, s56
	v_readlane_b32 s18, v253, 32
	v_readlane_b32 s19, v253, 33
	s_cselect_b32 s28, s95, s19
	s_cselect_b32 s29, s94, s18
	s_lshl_b64 s[20:21], s[20:21], 12
	s_add_u32 s20, s29, s20
	s_addc_u32 s21, s28, s21
	s_and_b32 s21, s21, 0xffff
	v_cvt_pk_f16_f32 v36, v26, v27
	v_cvt_pk_f16_f32 v37, v20, v21
	v_cvt_pk_f16_f32 v38, v30, v31
	v_cvt_pk_f16_f32 v39, v22, v23
	s_mov_b64 s[18:19], s[88:89]
	buffer_store_dwordx4 v[36:39], v1, s[20:23], 0 offen
	s_nop 1
	v_cvt_pk_f16_f32 v36, v32, v33
	v_cvt_pk_f16_f32 v37, v24, v25
	v_cvt_pk_f16_f32 v38, v34, v35
	v_cvt_pk_f16_f32 v39, v28, v29
	buffer_store_dwordx4 v[36:39], v101, s[20:23], 0 offen
	s_nop 0
